# baseline (speedup 1.0000x reference)
_Z11gemm_kernelILi128ELi192ELi1EEv8GemmArgs:
	s_load_dwordx2 s[4:5], s[0:1], 0x38
	s_load_dwordx2 s[22:23], s[0:1], 0x48
	s_load_dwordx2 s[24:25], s[0:1], 0x0
	s_load_dwordx2 s[26:27], s[0:1], 0x98
	s_addk_i32 s2, 0xe0
	s_mov_b32 s3, 0
	s_lshl_b64 s[6:7], s[2:3], 2
	s_waitcnt lgkmcnt(0)
	s_add_u32 s4, s4, s6
	s_addc_u32 s5, s5, s7
	s_load_dword s8, s[4:5], 0x0
	s_waitcnt lgkmcnt(0)
	s_cmp_lt_i32 s8, 0
	s_cbranch_scc1 .LBB3_4
	s_mov_b64 s[6:7], s[22:23]
	s_mov_b64 s[4:5], s[24:25]
	v_lshlrev_b32_e32 v64, 4, v0
	v_and_b32_e32 v1, 32, v0
	v_bitop3_b32 v1, v64, v1, 48 bitop3:0x6c
	s_and_b32 s2, s8, 0xffff
	v_bfe_u32 v4, v0, 2, 4
	v_lshrrev_b32_e32 v2, 1, v0
	v_lshrrev_b32_e32 v1, 1, v1
	v_lshrrev_b32_e32 v6, 3, v0
	v_and_or_b32 v1, v2, 32, v1
	v_add_u32_e32 v5, s2, v4
	v_and_b32_e32 v7, 48, v6
	s_movk_i32 s10, 0x70
	v_add_lshl_u32 v22, v5, v7, 12
	v_mov_b32_e32 v23, 0
	v_lshlrev_b32_e32 v44, 1, v1
	v_bitop3_b32 v1, v6, s10, 64 bitop3:0xc8
	s_waitcnt lgkmcnt(0)
	v_lshl_add_u64 v[2:3], s[4:5], 0, v[22:23]
	v_mov_b32_e32 v45, v23
	v_add_lshl_u32 v48, v5, v1, 12
	v_mov_b32_e32 v49, v23
	s_lshr_b32 s10, s8, 24
	s_bfe_u32 s9, s8, 0x80010
	v_lshl_add_u64 v[46:47], v[2:3], 0, v[44:45]
	v_lshl_add_u64 v[2:3], s[4:5], 0, v[48:49]
	s_mulk_i32 s10, 0x300
	v_lshl_add_u64 v[50:51], v[2:3], 0, v[44:45]
	s_mul_i32 s8, s9, 0xc0
	v_or_b32_e32 v2, s10, v4
	v_add_u32_e32 v4, s8, v2
	v_or_b32_e32 v2, v4, v7
	v_lshlrev_b32_e32 v52, 12, v2
	v_mov_b32_e32 v53, v23
	v_lshl_add_u64 v[2:3], s[6:7], 0, v[52:53]
	v_add_lshl_u32 v56, v4, v1, 12
	v_mov_b32_e32 v57, v23
	v_lshl_add_u64 v[54:55], v[2:3], 0, v[44:45]
	v_lshl_add_u64 v[2:3], s[6:7], 0, v[56:57]
	v_add_u32_e32 v60, 0x80000, v52
	v_mov_b32_e32 v61, v23
	v_lshl_add_u64 v[58:59], v[2:3], 0, v[44:45]
	v_lshl_add_u64 v[2:3], s[6:7], 0, v[60:61]
	v_lshl_add_u64 v[62:63], v[2:3], 0, v[44:45]
	v_readfirstlane_b32 s16, v0
	s_mov_b64 s[0:1], s[26:27]
	s_lshr_b32 s16, s16, 6
	s_lshl_b32 s16, s16, 10
	v_bfe_u32 v1, v0, 6, 2
	v_lshrrev_b32_e32 v80, 2, v0
	s_add_u32 m0, s16, 0
	s_nop 0
	global_load_lds_dwordx4 v[46:47], off
	s_add_u32 m0, s16, 8192
	s_nop 0
	global_load_lds_dwordx4 v[50:51], off
	s_add_u32 m0, s16, 16384
	s_nop 0
	global_load_lds_dwordx4 v[54:55], off
	s_add_u32 m0, s16, 24576
	s_nop 0
	global_load_lds_dwordx4 v[58:59], off
	s_add_u32 m0, s16, 32768
	s_nop 0
	global_load_lds_dwordx4 v[62:63], off
	s_add_u32 m0, s16, 40832
	s_nop 0
	global_load_lds_dwordx4 v[46:47], off offset:128
	s_add_u32 m0, s16, 49024
	s_nop 0
	global_load_lds_dwordx4 v[50:51], off offset:128
	s_add_u32 m0, s16, 57216
	s_nop 0
	global_load_lds_dwordx4 v[54:55], off offset:128
	s_add_u32 m0, s16, 65408
	s_nop 0
	global_load_lds_dwordx4 v[58:59], off offset:128
	s_add_u32 m0, s16, 73600
	s_nop 0
	global_load_lds_dwordx4 v[62:63], off offset:128
	s_add_u32 m0, s16, 81664
	s_nop 0
	global_load_lds_dwordx4 v[46:47], off offset:256
	s_add_u32 m0, s16, 89856
	s_nop 0
	global_load_lds_dwordx4 v[50:51], off offset:256
	s_add_u32 m0, s16, 98048
	s_nop 0
	global_load_lds_dwordx4 v[54:55], off offset:256
	s_add_u32 m0, s16, 106240
	s_nop 0
	global_load_lds_dwordx4 v[58:59], off offset:256
	s_add_u32 m0, s16, 114432
	s_nop 0
	global_load_lds_dwordx4 v[62:63], off offset:256
	s_mov_b32 s17, 0
	s_mov_b32 s18, 0xa000
	s_mov_b32 s19, 0x14000
	v_lshlrev_b32_e32 v25, 6, v0
	v_lshlrev_b32_e32 v27, 2, v0
	v_and_b32_e32 v24, 48, v0
	v_and_b32_e32 v25, 0x3c0, v25
	v_and_b32_e32 v27, 32, v27
	v_or_b32_e32 v26, v25, v24
	v_bitop3_b32 v87, v25, v27, v24 bitop3:0x36
	v_or_b32_e32 v24, v44, v60
	v_mov_b32_e32 v25, v23
	v_lshl_add_u64 v[24:25], s[6:7], 0, v[24:25]
	s_mov_b64 s[10:11], 0x100
	v_lshl_add_u64 v[70:71], v[24:25], 0, s[10:11]
	v_or_b32_e32 v24, v56, v44
	v_mov_b32_e32 v25, v23
	v_lshl_add_u64 v[24:25], s[6:7], 0, v[24:25]
	v_lshl_add_u64 v[72:73], v[24:25], 0, s[10:11]
	v_or_b32_e32 v24, v52, v44
	v_mov_b32_e32 v25, v23
	v_lshl_add_u64 v[24:25], s[6:7], 0, v[24:25]
	v_lshl_add_u64 v[74:75], v[24:25], 0, s[10:11]
	v_or_b32_e32 v24, v48, v44
	v_mov_b32_e32 v25, v23
	v_lshl_add_u64 v[24:25], s[4:5], 0, v[24:25]
	v_or_b32_e32 v22, v22, v44
	v_and_b32_e32 v81, 64, v80
	v_mul_u32_u24_e32 v86, 0x1800, v1
	v_lshl_add_u64 v[76:77], v[24:25], 0, s[10:11]
	v_lshl_add_u64 v[24:25], s[4:5], 0, v[22:23]
	v_bitop3_b32 v82, v26, v86, v27 bitop3:0xde
	v_lshlrev_b32_e32 v88, 7, v81
	v_lshl_add_u64 v[78:79], v[24:25], 0, s[10:11]
	s_mov_b64 s[4:5], 0x80
	v_mov_b32_e32 v22, v23
	v_mov_b32_e32 v24, v23
	v_mov_b32_e32 v25, v23
	v_mov_b32_e32 v50, v23
	v_mov_b32_e32 v51, v23
	v_mov_b32_e32 v52, v23
	v_mov_b32_e32 v54, v23
	v_mov_b32_e32 v55, v23
	v_mov_b32_e32 v56, v23
	v_mov_b32_e32 v58, v23
	v_mov_b32_e32 v59, v23
	v_mov_b32_e32 v60, v23
	v_mov_b32_e32 v66, v23
	v_mov_b32_e32 v67, v23
	v_mov_b32_e32 v68, v23
	v_mov_b32_e32 v69, v23
	v_mov_b32_e32 v62, v23
	v_mov_b32_e32 v63, v23
	v_mov_b32_e32 v64, v23
	v_mov_b32_e32 v65, v23
	v_mov_b32_e32 v42, v23
	v_mov_b32_e32 v43, v23
	v_mov_b32_e32 v44, v23
	v_mov_b32_e32 v46, v23
	v_mov_b32_e32 v47, v23
	v_mov_b32_e32 v48, v23
	v_mov_b32_e32 v30, v23
	v_mov_b32_e32 v31, v23
	v_mov_b32_e32 v32, v23
	v_mov_b32_e32 v33, v23
	v_mov_b32_e32 v34, v23
	v_mov_b32_e32 v35, v23
	v_mov_b32_e32 v36, v23
	v_mov_b32_e32 v37, v23
	v_mov_b32_e32 v38, v23
	v_mov_b32_e32 v39, v23
	v_mov_b32_e32 v40, v23
	v_mov_b32_e32 v41, v23
	v_mov_b32_e32 v26, v23
	v_mov_b32_e32 v27, v23
	v_mov_b32_e32 v28, v23
	v_mov_b32_e32 v29, v23
	v_add_u32_e32 v146, v87, v88
	s_waitcnt vmcnt(10) lgkmcnt(0)
	s_barrier
	ds_read_b128 v[90:93], v146
	ds_read_b128 v[106:109], v82 offset:16384
	ds_read_b128 v[110:113], v82 offset:18432
	ds_read_b128 v[114:117], v82 offset:20480
	ds_read_b128 v[94:97], v146 offset:2048
	ds_read_b128 v[98:101], v146 offset:4096
	ds_read_b128 v[102:105], v146 offset:6144
